# barrier-hosted expert weight conversion + pipelined x->fp8 loop + accumulator zeroing removed + generic fallback for uncovered tiles
# baseline (speedup 1.0000x reference)
.LBB0_15:
	s_or_b64 exec, exec, s[6:7]
	s_ashr_i32 s0, s2, 6
	v_readlane_b32 s1, v239, 23
	s_add_i32 s3, s0, s1
	v_readlane_b32 s38, v239, 11
	v_readlane_b32 s39, v239, 12
	v_readlane_b32 s40, v239, 15
	v_readlane_b32 s41, v239, 16
	v_and_b32_e32 v20, 63, v2
	v_lshlrev_b32_e32 v1, 2, v20
	v_and_b32_e32 v100, 60, v20
	v_and_b32_e32 v101, 3, v20
	v_lshlrev_b32_e32 v101, 4, v101
	s_mov_b32 s42, 0xaaaaaaaa
	s_mov_b32 s43, 0xaaaaaaaa
	s_mov_b32 s44, 0x55555555
	s_mov_b32 s45, 0x55555555
	s_mov_b32 s46, 0xcccccccc
	s_mov_b32 s47, 0xcccccccc
	s_mov_b32 s48, 0x33333333
	s_mov_b32 s49, 0x33333333
	s_mov_b32 s19, 0
	s_movk_i32 s20, 2047
.Lp0w_loop:
	s_cmp_gt_u32 s3, s20
	s_cbranch_scc0 .Lp0w_work
	s_cmp_lg_u32 s19, 0
	s_cbranch_scc1 .LBB0_50
	s_mov_b32 s19, 1
	s_movk_i32 s20, 26623
	s_mul_i32 s3, s74, 96
	s_ashr_i32 s0, s2, 6
	v_readlane_b32 s1, v239, 23
	s_add_i32 s3, s3, s0
	s_add_i32 s3, s3, s1
	s_add_i32 s3, s3, 2048
	s_branch .Lp0w_loop
.Lp0w_work:
	s_mov_b32 s13, s3
	s_cmp_lt_u32 s13, 1472
	s_cbranch_scc0 .Lp0w_t1
	s_mul_i32 s14, s13, 45591
	s_lshr_b32 s14, s14, 22
	s_mul_i32 s15, s14, 92
	s_sub_i32 s15, s13, s15
	s_mul_i32 s16, s14, 1507328
	s_lshl_b32 s0, s15, 8
	s_add_i32 s16, s16, s0
	s_lshl_b32 s17, s15, 16
	s_lshl_b32 s0, s14, 6
	s_add_i32 s17, s17, s0
	s_add_i32 s17, s17, 0x200000
	s_mov_b64 s[36:37], s[82:83]
	s_mov_b32 s8, 23552
	s_movk_i32 s12, 1024
	s_branch .Lp0w_plain
